# lru prep: LDS reads of the conv and gate steps hoisted (one wait instead of 32 round trips), on top of stage 1b rewrite
# speedup vs baseline: 1.0002x; 1.0002x over previous
.LBB0_370:
	v_ashrrev_i32_e32 v11, 6, v30
	v_add_u32_e32 v8, v111, v104
	s_waitcnt lgkmcnt(0)
	s_barrier
	v_lshl_add_u32 v22, v11, 8, v8
	ds_read2st64_b32 v[112:113], v22 offset1:1
	ds_read2st64_b32 v[114:115], v22 offset0:2 offset1:3
	ds_read2st64_b32 v[116:117], v22 offset0:8 offset1:9
	ds_read2st64_b32 v[118:119], v22 offset0:10 offset1:11
	ds_read2st64_b32 v[120:121], v22 offset0:16 offset1:17
	ds_read2st64_b32 v[122:123], v22 offset0:18 offset1:19
	ds_read2st64_b32 v[124:125], v22 offset0:24 offset1:25
	ds_read2st64_b32 v[126:127], v22 offset0:26 offset1:27
	ds_read2st64_b32 v[128:129], v22 offset0:32 offset1:33
	ds_read2st64_b32 v[130:131], v22 offset0:34 offset1:35
	ds_read2st64_b32 v[132:133], v22 offset0:40 offset1:41
	ds_read2st64_b32 v[134:135], v22 offset0:42 offset1:43
	ds_read2st64_b32 v[136:137], v22 offset0:48 offset1:49
	ds_read2st64_b32 v[138:139], v22 offset0:50 offset1:51
	ds_read2st64_b32 v[140:141], v22 offset0:56 offset1:57
	ds_read2st64_b32 v[142:143], v22 offset0:58 offset1:59
	v_lshlrev_b32_e32 v9, 1, v31
	s_movk_i32 s0, 0x104
	v_sub_u32_e32 v10, v8, v9
	v_mad_u64_u32 v[8:9], s[0:1], v11, s0, v[8:9]
	s_waitcnt vmcnt(12) lgkmcnt(0)
	v_fma_f32 v23, v15, v112, v14
	v_fmac_f32_e32 v23, v21, v113
	v_mad_u64_u32 v[10:11], s[0:1], v11, s39, v[10:11]
	s_or_b32 s0, s24, s71
	s_ashr_i32 s1, s0, 31
	v_fmac_f32_e32 v23, v12, v114
	v_fmac_f32_e32 v23, v13, v115
	ds_write_b32 v8, v23 offset:17408
	v_bfe_u32 v9, v23, 16, 1
	v_add3_u32 v9, v23, v9, s25
	ds_write_b16_d16_hi v10, v9 offset:34304
	s_lshl_b64 s[0:1], s[0:1], 13
	v_fma_f32 v9, v15, v116, v14
	v_fmac_f32_e32 v9, v21, v117
	s_add_u32 s2, s69, s0
	s_addc_u32 s3, s70, s1
	v_and_b32_e32 v24, 48, v30
	v_mov_b32_e32 v25, v105
	v_fmac_f32_e32 v9, v12, v118
	v_fmac_f32_e32 v9, v13, v119
	ds_write_b32 v8, v9 offset:19488
	v_bfe_u32 v11, v9, 16, 1
	v_add3_u32 v9, v9, v11, s25
	ds_write_b16_d16_hi v10, v9 offset:35456
	s_or_b32 s0, s24, s72
	v_fma_f32 v9, v15, v120, v14
	v_fmac_f32_e32 v9, v21, v121
	s_ashr_i32 s1, s0, 31
	s_lshl_b64 s[0:1], s[0:1], 13
	s_add_u32 s0, s69, s0
	s_addc_u32 s1, s70, s1
	v_fmac_f32_e32 v9, v12, v122
	v_fmac_f32_e32 v9, v13, v123
	ds_write_b32 v8, v9 offset:21568
	v_bfe_u32 v11, v9, 16, 1
	v_add3_u32 v9, v9, v11, s25
	ds_write_b16_d16_hi v10, v9 offset:36608
	s_mov_b32 s14, 0xbfb8aa3b
	v_fma_f32 v9, v15, v124, v14
	v_fmac_f32_e32 v9, v21, v125
	v_or_b32_e32 v47, 16, v35
	v_cmp_gt_u32_e32 vcc, s21, v30
	v_mov_b32_e32 v67, 1.0
	v_mov_b32_e32 v68, 0
	v_fmac_f32_e32 v9, v12, v126
	v_fmac_f32_e32 v9, v13, v127
	ds_write_b32 v8, v9 offset:23648
	v_bfe_u32 v11, v9, 16, 1
	v_add3_u32 v9, v9, v11, s25
	ds_write_b16_d16_hi v10, v9 offset:37760
	v_fma_f32 v9, v15, v128, v14
	v_fmac_f32_e32 v9, v21, v129
	v_fmac_f32_e32 v9, v12, v130
	v_fmac_f32_e32 v9, v13, v131
	ds_write_b32 v8, v9 offset:25728
	v_bfe_u32 v11, v9, 16, 1
	v_add3_u32 v9, v9, v11, s25
	ds_write_b16_d16_hi v10, v9 offset:38912
	v_fma_f32 v9, v15, v132, v14
	v_fmac_f32_e32 v9, v21, v133
	v_fmac_f32_e32 v9, v12, v134
	v_fmac_f32_e32 v9, v13, v135
	ds_write_b32 v8, v9 offset:27808
	v_bfe_u32 v11, v9, 16, 1
	v_add3_u32 v9, v9, v11, s25
	ds_write_b16_d16_hi v10, v9 offset:40064
	v_fma_f32 v9, v15, v136, v14
	v_fmac_f32_e32 v9, v21, v137
	v_fmac_f32_e32 v9, v12, v138
	v_fmac_f32_e32 v9, v13, v139
	ds_write_b32 v8, v9 offset:29888
	v_bfe_u32 v11, v9, 16, 1
	v_add3_u32 v9, v9, v11, s25
	ds_write_b16_d16_hi v10, v9 offset:41216
	v_fmac_f32_e32 v14, v15, v140
	v_fmac_f32_e32 v14, v21, v141
	v_fmac_f32_e32 v14, v12, v142
	v_fmac_f32_e32 v14, v13, v143
	ds_write_b32 v8, v14 offset:31968
	v_bfe_u32 v8, v14, 16, 1
	v_add3_u32 v8, v14, v8, s25
	v_lshrrev_b32_e32 v16, 2, v30
	ds_write_b16_d16_hi v10, v8 offset:42368
	v_or_b32_e32 v8, s34, v35
	v_and_or_b32 v21, v16, 12, s34
	v_lshlrev_b32_e32 v16, 7, v35
	v_mov_b32_e32 v17, v105
	v_mul_u32_u24_e32 v8, 0x90, v8
	v_lshl_add_u64 v[22:23], s[2:3], 0, v[16:17]
	s_waitcnt lgkmcnt(0)
	s_barrier
	v_add3_u32 v8, v111, v8, v24
	v_lshl_add_u64 v[22:23], v[22:23], 0, v[24:25]
	ds_read_b128 v[12:15], v8 offset:34304
	ds_read_b128 v[8:11], v8 offset:34368
	global_load_dwordx4 v[36:39], v[22:23], off
	global_load_dwordx4 v[48:51], v[22:23], off offset:64
	v_lshl_add_u64 v[16:17], s[0:1], 0, v[16:17]
	v_lshl_add_u64 v[16:17], v[16:17], 0, v[24:25]
	v_lshlrev_b32_e32 v42, 6, v21
	s_waitcnt vmcnt(1) lgkmcnt(1)
	v_mfma_f32_16x16x32_bf16 v[36:39], v[12:15], v[36:39], 0
	global_load_dwordx4 v[52:55], v[16:17], off offset:64
	s_waitcnt vmcnt(1) lgkmcnt(0)
	v_mfma_f32_16x16x32_bf16 v[48:51], v[8:11], v[48:51], v[36:39]
	s_nop 4
	global_load_dwordx4 v[36:39], v[16:17], off
	v_mul_f32_e64 v17, |v20|, s14
	s_nop 0
	v_add_f32_e32 v22, v18, v48
	v_mul_f32_e32 v22, 0xbfb8aa3b, v22
	v_exp_f32_e32 v17, v17
	v_exp_f32_e32 v22, v22
	v_max_f32_e64 v16, -v20, -v20
	v_max_f32_e32 v16, 0, v16
	v_add_f32_e32 v17, 1.0, v17
	v_add_f32_e32 v22, 1.0, v22
	v_log_f32_e32 v17, v17
	v_rcp_f32_e32 v22, v22
	v_or_b32_e32 v20, s73, v35
	v_lshlrev_b32_e32 v48, 7, v47
	v_fmac_f32_e32 v16, 0x3f317218, v17
	v_mul_f32_e32 v22, 0xc1000000, v22
	v_mul_f32_e32 v22, v16, v22
	v_mul_f32_e32 v22, 0x3fb8aa3b, v22
	v_exp_f32_e32 v22, v22
	v_lshlrev_b32_e32 v17, 2, v35
	s_waitcnt vmcnt(0)
	v_mfma_f32_16x16x32_bf16 v[36:39], v[12:15], v[36:39], 0
	v_mfma_f32_16x16x32_bf16 v[52:55], v[8:11], v[52:55], v[36:39]
	s_nop 6
	v_fma_f32 v36, -v22, v22, 1.0
	v_max_f32_e32 v36, 0, v36
	v_add_f32_e32 v23, v19, v52
	v_mul_f32_e32 v23, 0xbfb8aa3b, v23
	v_exp_f32_e32 v23, v23
	v_sqrt_f32_e32 v36, v36
	v_or_b32_e32 v39, 64, v42
	v_or_b32_e32 v38, 0x80, v42
	v_add_f32_e32 v23, 1.0, v23
	v_rcp_f32_e32 v23, v23
	v_or_b32_e32 v37, 0xc0, v42
	v_mul_f32_e32 v23, v23, v36
	v_mul_u32_u24_e32 v36, 0x104, v21
	v_add3_u32 v36, v111, v17, v36
	ds_read_b32 v144, v36 offset:17408
	ds_read_b32 v145, v36 offset:17668
	ds_read_b32 v146, v36 offset:17928
	ds_read_b32 v147, v36 offset:18188
	ds_read_b32 v148, v36 offset:17472
	ds_read_b32 v149, v36 offset:17732
	ds_read_b32 v150, v36 offset:17992
	ds_read_b32 v151, v36 offset:18252
	ds_read_b32 v152, v36 offset:17536
	ds_read_b32 v153, v36 offset:17796
	ds_read_b32 v154, v36 offset:18056
	ds_read_b32 v155, v36 offset:18316
	ds_read_b32 v156, v36 offset:17600
	ds_read_b32 v157, v36 offset:17860
	ds_read_b32 v158, v36 offset:18120
	ds_read_b32 v159, v36 offset:18380
	v_or_b32_e32 v21, v42, v20
	v_lshlrev_b32_e32 v21, 2, v21
	s_waitcnt lgkmcnt(0)
	v_mul_f32_e32 v17, v144, v23
	v_add_u32_e32 v23, v111, v21
	v_add_u32_e32 v21, v28, v21
	ds_write_b32 v23, v22 offset:43520
	ds_write_b32 v21, v17
	v_add_f32_e32 v17, v18, v49
	v_mul_f32_e32 v17, 0xbfb8aa3b, v17
	v_exp_f32_e32 v17, v17
	v_add_f32_e32 v21, v19, v53
	v_mul_f32_e32 v21, 0xbfb8aa3b, v21
	v_exp_f32_e32 v21, v21
	v_add_f32_e32 v17, 1.0, v17
	v_rcp_f32_e32 v17, v17
	v_mov_b32_e32 v49, v105
	v_add_f32_e32 v21, 1.0, v21
	v_rcp_f32_e32 v21, v21
	v_mul_f32_e32 v17, 0xc1000000, v17
	v_mul_f32_e32 v17, v16, v17
	v_mul_f32_e32 v17, 0x3fb8aa3b, v17
	v_exp_f32_e32 v17, v17
	s_nop 0
	v_fma_f32 v22, -v17, v17, 1.0
	v_max_f32_e32 v22, 0, v22
	v_sqrt_f32_e32 v22, v22
	s_nop 0
	v_mul_f32_e32 v21, v21, v22
	v_mul_f32_e32 v21, v145, v21
	v_or_b32_e32 v22, v39, v20
	v_lshlrev_b32_e32 v22, 2, v22
	v_add_u32_e32 v23, v111, v22
	ds_write_b32 v23, v17 offset:43520
	v_add_u32_e32 v17, v28, v22
	ds_write_b32 v17, v21
	v_add_f32_e32 v17, v18, v50
	v_mul_f32_e32 v17, 0xbfb8aa3b, v17
	v_exp_f32_e32 v17, v17
	v_add_f32_e32 v21, v19, v54
	v_mul_f32_e32 v21, 0xbfb8aa3b, v21
	v_exp_f32_e32 v21, v21
	v_add_f32_e32 v17, 1.0, v17
	v_rcp_f32_e32 v17, v17
	v_add_f32_e32 v21, 1.0, v21
	v_rcp_f32_e32 v21, v21
	v_mul_f32_e32 v17, 0xc1000000, v17
	v_mul_f32_e32 v17, v16, v17
	v_mul_f32_e32 v17, 0x3fb8aa3b, v17
	v_exp_f32_e32 v17, v17
	s_nop 0
	v_fma_f32 v22, -v17, v17, 1.0
	v_max_f32_e32 v22, 0, v22
	v_sqrt_f32_e32 v22, v22
	s_nop 0
	v_mul_f32_e32 v21, v21, v22
	v_mul_f32_e32 v21, v146, v21
	v_or_b32_e32 v22, v38, v20
	v_lshlrev_b32_e32 v22, 2, v22
	v_add_u32_e32 v23, v111, v22
	ds_write_b32 v23, v17 offset:43520
	v_add_u32_e32 v17, v28, v22
	ds_write_b32 v17, v21
	v_add_f32_e32 v17, v18, v51
	v_mul_f32_e32 v17, 0xbfb8aa3b, v17
	v_exp_f32_e32 v17, v17
	v_add_f32_e32 v18, v19, v55
	v_mul_f32_e32 v18, 0xbfb8aa3b, v18
	v_exp_f32_e32 v18, v18
	v_add_f32_e32 v17, 1.0, v17
	v_rcp_f32_e32 v17, v17
	v_add_f32_e32 v18, 1.0, v18
	v_rcp_f32_e32 v18, v18
	v_mul_f32_e32 v17, 0xc1000000, v17
	v_mul_f32_e32 v16, v16, v17
	v_mul_f32_e32 v16, 0x3fb8aa3b, v16
	v_exp_f32_e32 v16, v16
	s_nop 0
	v_fma_f32 v17, -v16, v16, 1.0
	v_max_f32_e32 v17, 0, v17
	v_sqrt_f32_e32 v17, v17
	s_nop 0
	v_mul_f32_e32 v17, v18, v17
	v_mul_f32_e32 v17, v147, v17
	v_or_b32_e32 v18, v37, v20
	v_lshlrev_b32_e32 v18, 2, v18
	v_add_u32_e32 v19, v111, v18
	ds_write_b32 v19, v16 offset:43520
	v_add_u32_e32 v16, v28, v18
	ds_write_b32 v16, v17
	v_lshl_add_u64 v[16:17], s[2:3], 0, v[48:49]
	v_lshl_add_u64 v[20:21], v[16:17], 0, v[24:25]
	global_load_dwordx4 v[16:19], v[20:21], off
	s_waitcnt vmcnt(0)
	v_mfma_f32_16x16x32_bf16 v[16:19], v[12:15], v[16:19], 0
	global_load_dwordx4 v[20:23], v[20:21], off offset:64
	s_waitcnt vmcnt(0)
	v_mfma_f32_16x16x32_bf16 v[16:19], v[8:11], v[20:23], v[16:19]
	v_lshl_add_u64 v[20:21], s[0:1], 0, v[48:49]
	v_lshl_add_u64 v[48:49], v[20:21], 0, v[24:25]
	global_load_dwordx4 v[20:23], v[48:49], off
	s_waitcnt vmcnt(0)
	v_mfma_f32_16x16x32_bf16 v[20:23], v[12:15], v[20:23], 0
	global_load_dwordx4 v[48:51], v[48:49], off offset:64
	s_nop 1
	v_add_f32_e32 v16, v45, v16
	v_mul_f32_e32 v16, 0xbfb8aa3b, v16
	s_waitcnt vmcnt(0)
	v_mfma_f32_16x16x32_bf16 v[20:23], v[8:11], v[48:51], v[20:23]
	v_max_f32_e64 v48, -v46, -v46
	v_mul_f32_e64 v46, |v46|, s14
	v_exp_f32_e32 v46, v46
	v_exp_f32_e32 v16, v16
	v_max_f32_e32 v49, 0, v48
	s_nop 2
	v_add_f32_e32 v20, v44, v20
	v_add_f32_e32 v46, 1.0, v46
	v_add_f32_e32 v16, 1.0, v16
	v_log_f32_e32 v46, v46
	v_rcp_f32_e32 v16, v16
	v_mul_f32_e32 v20, 0xbfb8aa3b, v20
	v_exp_f32_e32 v20, v20
	v_fmac_f32_e32 v49, 0x3f317218, v46
	v_mul_f32_e32 v16, 0xc1000000, v16
	v_mul_f32_e32 v16, v49, v16
	v_mul_f32_e32 v16, 0x3fb8aa3b, v16
	v_exp_f32_e32 v16, v16
	v_add_f32_e32 v20, 1.0, v20
	v_rcp_f32_e32 v20, v20
	v_add_u32_e32 v51, s73, v35
	v_fma_f32 v46, -v16, v16, 1.0
	v_max_f32_e32 v46, 0, v46
	v_sqrt_f32_e32 v46, v46
	v_or_b32_e32 v50, s73, v47
	v_add_u32_e32 v47, v42, v51
	v_lshl_add_u32 v48, v47, 2, v111
	v_mul_f32_e32 v20, v20, v46
	ds_write_b32 v48, v16 offset:43584
	v_mul_f32_e32 v20, v148, v20
	v_or_b32_e32 v46, v42, v50
	v_lshl_add_u32 v16, v46, 2, v28
	ds_write_b32 v16, v20
	v_add_f32_e32 v16, v45, v17
	v_mul_f32_e32 v16, 0xbfb8aa3b, v16
	v_exp_f32_e32 v16, v16
	v_add_f32_e32 v17, v44, v21
	v_mul_f32_e32 v17, 0xbfb8aa3b, v17
	v_exp_f32_e32 v17, v17
	v_add_f32_e32 v16, 1.0, v16
	v_rcp_f32_e32 v16, v16
	v_add_u32_e32 v21, v39, v51
	v_add_f32_e32 v17, 1.0, v17
	v_rcp_f32_e32 v17, v17
	v_mul_f32_e32 v16, 0xc1000000, v16
	v_mul_f32_e32 v16, v49, v16
	v_mul_f32_e32 v16, 0x3fb8aa3b, v16
	v_exp_f32_e32 v16, v16
	v_lshl_add_u32 v47, v21, 2, v111
	v_fma_f32 v20, -v16, v16, 1.0
	v_max_f32_e32 v20, 0, v20
	v_sqrt_f32_e32 v20, v20
	s_nop 0
	v_mul_f32_e32 v17, v17, v20
	ds_write_b32 v47, v16 offset:43584
	v_mul_f32_e32 v17, v149, v17
	v_or_b32_e32 v20, v39, v50
	v_lshl_add_u32 v16, v20, 2, v28
	ds_write_b32 v16, v17
	v_add_f32_e32 v16, v45, v18
	v_mul_f32_e32 v16, 0xbfb8aa3b, v16
	v_exp_f32_e32 v16, v16
	v_add_f32_e32 v17, v44, v22
	v_mul_f32_e32 v17, 0xbfb8aa3b, v17
	v_exp_f32_e32 v17, v17
	v_add_f32_e32 v16, 1.0, v16
	v_rcp_f32_e32 v16, v16
	v_add_u32_e32 v20, v38, v51
	v_add_f32_e32 v17, 1.0, v17
	v_rcp_f32_e32 v17, v17
	v_mul_f32_e32 v16, 0xc1000000, v16
	v_mul_f32_e32 v16, v49, v16
	v_mul_f32_e32 v16, 0x3fb8aa3b, v16
	v_exp_f32_e32 v16, v16
	v_lshl_add_u32 v46, v20, 2, v111
	v_fma_f32 v18, -v16, v16, 1.0
	v_max_f32_e32 v18, 0, v18
	v_sqrt_f32_e32 v18, v18
	s_nop 0
	v_mul_f32_e32 v17, v17, v18
	ds_write_b32 v46, v16 offset:43584
	v_mul_f32_e32 v17, v150, v17
	v_or_b32_e32 v18, v38, v50
	v_lshl_add_u32 v16, v18, 2, v28
	ds_write_b32 v16, v17
	v_add_f32_e32 v16, v45, v19
	v_mul_f32_e32 v16, 0xbfb8aa3b, v16
	v_exp_f32_e32 v16, v16
	v_add_f32_e32 v17, v44, v23
	v_mul_f32_e32 v17, 0xbfb8aa3b, v17
	v_exp_f32_e32 v17, v17
	v_add_f32_e32 v16, 1.0, v16
	v_rcp_f32_e32 v16, v16
	v_add_u32_e32 v19, v37, v51
	v_add_f32_e32 v17, 1.0, v17
	v_rcp_f32_e32 v17, v17
	v_mul_f32_e32 v16, 0xc1000000, v16
	v_mul_f32_e32 v16, v49, v16
	v_mul_f32_e32 v16, 0x3fb8aa3b, v16
	v_exp_f32_e32 v16, v16
	v_lshl_add_u32 v44, v19, 2, v111
	v_or_b32_e32 v45, 32, v35
	v_mov_b32_e32 v51, v105
	v_fma_f32 v18, -v16, v16, 1.0
	v_max_f32_e32 v18, 0, v18
	v_sqrt_f32_e32 v18, v18
	v_max_f32_e64 v49, -v43, -v43
	v_mul_f32_e64 v43, |v43|, s14
	v_exp_f32_e32 v43, v43
	v_mul_f32_e32 v17, v17, v18
	ds_write_b32 v44, v16 offset:43584
	v_add_f32_e32 v43, 1.0, v43
	v_log_f32_e32 v43, v43
	v_max_f32_e32 v49, 0, v49
	v_mul_f32_e32 v17, v151, v17
	v_or_b32_e32 v18, v37, v50
	v_lshl_add_u32 v16, v18, 2, v28
	v_lshlrev_b32_e32 v50, 7, v45
	ds_write_b32 v16, v17
	v_lshl_add_u64 v[16:17], s[2:3], 0, v[50:51]
	v_lshl_add_u64 v[20:21], v[16:17], 0, v[24:25]
	global_load_dwordx4 v[16:19], v[20:21], off
	s_waitcnt vmcnt(0)
	v_mfma_f32_16x16x32_bf16 v[16:19], v[12:15], v[16:19], 0
	global_load_dwordx4 v[20:23], v[20:21], off offset:64
	v_fmac_f32_e32 v49, 0x3f317218, v43
	v_or_b32_e32 v43, s73, v45
	s_waitcnt vmcnt(0)
	v_mfma_f32_16x16x32_bf16 v[16:19], v[8:11], v[20:23], v[16:19]
	v_lshl_add_u64 v[20:21], s[0:1], 0, v[50:51]
	v_lshl_add_u64 v[50:51], v[20:21], 0, v[24:25]
	global_load_dwordx4 v[20:23], v[50:51], off
	s_nop 4
	v_add_f32_e32 v16, v41, v16
	global_load_dwordx4 v[50:53], v[50:51], off offset:64
	v_mul_f32_e32 v16, 0xbfb8aa3b, v16
	v_exp_f32_e32 v16, v16
	s_waitcnt vmcnt(1)
	v_mfma_f32_16x16x32_bf16 v[20:23], v[12:15], v[20:23], 0
	v_add_f32_e32 v16, 1.0, v16
	v_rcp_f32_e32 v16, v16
	v_or_b32_e32 v35, 48, v35
	s_waitcnt vmcnt(0)
	v_mfma_f32_16x16x32_bf16 v[20:23], v[8:11], v[50:53], v[20:23]
	v_mul_f32_e32 v16, 0xc1000000, v16
	v_mul_f32_e32 v16, v49, v16
	v_mul_f32_e32 v16, 0x3fb8aa3b, v16
	v_exp_f32_e32 v16, v16
	s_nop 3
	v_add_f32_e32 v20, v40, v20
	v_mul_f32_e32 v20, 0xbfb8aa3b, v20
	v_exp_f32_e32 v20, v20
	v_fma_f32 v45, -v16, v16, 1.0
	v_max_f32_e32 v45, 0, v45
	v_sqrt_f32_e32 v45, v45
	v_add_f32_e32 v20, 1.0, v20
	v_rcp_f32_e32 v20, v20
	s_nop 0
	v_mul_f32_e32 v20, v20, v45
	ds_write_b32 v48, v16 offset:43648
	v_mul_f32_e32 v20, v152, v20
	v_or_b32_e32 v45, v42, v43
	v_lshl_add_u32 v16, v45, 2, v28
	ds_write_b32 v16, v20
	v_add_f32_e32 v16, v41, v17
	v_mul_f32_e32 v16, 0xbfb8aa3b, v16
	v_exp_f32_e32 v16, v16
	v_add_f32_e32 v17, v40, v21
	v_mul_f32_e32 v17, 0xbfb8aa3b, v17
	v_exp_f32_e32 v17, v17
	v_add_f32_e32 v16, 1.0, v16
	v_rcp_f32_e32 v16, v16
	v_add_f32_e32 v17, 1.0, v17
	v_rcp_f32_e32 v17, v17
	v_mul_f32_e32 v16, 0xc1000000, v16
	v_mul_f32_e32 v16, v49, v16
	v_mul_f32_e32 v16, 0x3fb8aa3b, v16
	v_exp_f32_e32 v16, v16
	s_nop 0
	v_fma_f32 v20, -v16, v16, 1.0
	v_max_f32_e32 v20, 0, v20
	v_sqrt_f32_e32 v20, v20
	s_nop 0
	v_mul_f32_e32 v17, v17, v20
	ds_write_b32 v47, v16 offset:43648
	v_mul_f32_e32 v17, v153, v17
	v_or_b32_e32 v20, v39, v43
	v_lshl_add_u32 v16, v20, 2, v28
	ds_write_b32 v16, v17
	v_add_f32_e32 v16, v41, v18
	v_mul_f32_e32 v16, 0xbfb8aa3b, v16
	v_exp_f32_e32 v16, v16
	v_add_f32_e32 v17, v40, v22
	v_mul_f32_e32 v17, 0xbfb8aa3b, v17
	v_exp_f32_e32 v17, v17
	v_add_f32_e32 v16, 1.0, v16
	v_rcp_f32_e32 v16, v16
	v_add_f32_e32 v17, 1.0, v17
	v_rcp_f32_e32 v17, v17
	v_mul_f32_e32 v16, 0xc1000000, v16
	v_mul_f32_e32 v16, v49, v16
	v_mul_f32_e32 v16, 0x3fb8aa3b, v16
	v_exp_f32_e32 v16, v16
	s_nop 0
	v_fma_f32 v18, -v16, v16, 1.0
	v_max_f32_e32 v18, 0, v18
	v_sqrt_f32_e32 v18, v18
	s_nop 0
	v_mul_f32_e32 v17, v17, v18
	ds_write_b32 v46, v16 offset:43648
	v_mul_f32_e32 v17, v154, v17
	v_or_b32_e32 v18, v38, v43
	v_lshl_add_u32 v16, v18, 2, v28
	ds_write_b32 v16, v17
	v_add_f32_e32 v16, v41, v19
	v_mul_f32_e32 v16, 0xbfb8aa3b, v16
	v_exp_f32_e32 v16, v16
	v_add_f32_e32 v17, v40, v23
	v_mul_f32_e32 v17, 0xbfb8aa3b, v17
	v_exp_f32_e32 v17, v17
	v_add_f32_e32 v16, 1.0, v16
	v_rcp_f32_e32 v16, v16
	v_lshlrev_b32_e32 v40, 7, v35
	v_add_f32_e32 v17, 1.0, v17
	v_rcp_f32_e32 v17, v17
	v_mul_f32_e32 v16, 0xc1000000, v16
	v_mul_f32_e32 v16, v49, v16
	v_mul_f32_e32 v16, 0x3fb8aa3b, v16
	v_exp_f32_e32 v16, v16
	v_mov_b32_e32 v41, v105
	v_fma_f32 v18, -v16, v16, 1.0
	v_max_f32_e32 v18, 0, v18
	v_sqrt_f32_e32 v18, v18
	s_nop 0
	v_mul_f32_e32 v17, v17, v18
	ds_write_b32 v44, v16 offset:43648
	v_mul_f32_e32 v17, v155, v17
	v_or_b32_e32 v18, v37, v43
	v_lshl_add_u32 v16, v18, 2, v28
	ds_write_b32 v16, v17
	v_lshl_add_u64 v[16:17], s[2:3], 0, v[40:41]
	v_lshl_add_u64 v[20:21], v[16:17], 0, v[24:25]
	global_load_dwordx4 v[16:19], v[20:21], off
	s_waitcnt vmcnt(0)
	v_mfma_f32_16x16x32_bf16 v[16:19], v[12:15], v[16:19], 0
	global_load_dwordx4 v[20:23], v[20:21], off offset:64
	s_waitcnt vmcnt(0)
	v_mfma_f32_16x16x32_bf16 v[16:19], v[8:11], v[20:23], v[16:19]
	v_lshl_add_u64 v[20:21], s[0:1], 0, v[40:41]
	v_lshl_add_u64 v[24:25], v[20:21], 0, v[24:25]
	global_load_dwordx4 v[20:23], v[24:25], off
	s_waitcnt vmcnt(0)
	v_mfma_f32_16x16x32_bf16 v[12:15], v[12:15], v[20:23], 0
	global_load_dwordx4 v[20:23], v[24:25], off offset:64
	s_waitcnt vmcnt(0)
	v_mfma_f32_16x16x32_bf16 v[8:11], v[8:11], v[20:23], v[12:15]
	s_nop 4
	v_add_f32_e32 v14, v33, v16
	v_mul_f32_e64 v13, |v34|, s14
	v_mul_f32_e32 v14, 0xbfb8aa3b, v14
	v_exp_f32_e32 v13, v13
	v_exp_f32_e32 v14, v14
	v_max_f32_e64 v12, -v34, -v34
	v_max_f32_e32 v12, 0, v12
	v_add_f32_e32 v13, 1.0, v13
	v_add_f32_e32 v14, 1.0, v14
	v_log_f32_e32 v13, v13
	v_rcp_f32_e32 v14, v14
	v_add_f32_e32 v8, v32, v8
	v_mul_f32_e32 v8, 0xbfb8aa3b, v8
	v_fmac_f32_e32 v12, 0x3f317218, v13
	v_mul_f32_e32 v14, 0xc1000000, v14
	v_mul_f32_e32 v14, v12, v14
	v_mul_f32_e32 v14, 0x3fb8aa3b, v14
	v_exp_f32_e32 v14, v14
	v_exp_f32_e32 v8, v8
	v_or_b32_e32 v13, s73, v35
	v_add_f32_e32 v9, v32, v9
	v_fma_f32 v15, -v14, v14, 1.0
	v_add_f32_e32 v8, 1.0, v8
	v_max_f32_e32 v15, 0, v15
	v_rcp_f32_e32 v8, v8
	v_sqrt_f32_e32 v15, v15
	v_mul_f32_e32 v9, 0xbfb8aa3b, v9
	v_exp_f32_e32 v9, v9
	v_mul_f32_e32 v8, v8, v15
	ds_write_b32 v48, v14 offset:43712
	v_add_f32_e32 v9, 1.0, v9
	v_rcp_f32_e32 v9, v9
	v_mul_f32_e32 v8, v156, v8
	v_or_b32_e32 v15, v42, v13
	v_lshl_add_u32 v14, v15, 2, v28
	ds_write_b32 v14, v8
	v_add_f32_e32 v8, v33, v17
	v_mul_f32_e32 v8, 0xbfb8aa3b, v8
	v_exp_f32_e32 v8, v8
	s_nop 0
	v_add_f32_e32 v8, 1.0, v8
	v_rcp_f32_e32 v8, v8
	s_nop 0
	v_mul_f32_e32 v8, 0xc1000000, v8
	v_mul_f32_e32 v8, v12, v8
	v_mul_f32_e32 v8, 0x3fb8aa3b, v8
	v_exp_f32_e32 v8, v8
	s_nop 0
	v_fma_f32 v14, -v8, v8, 1.0
	v_max_f32_e32 v14, 0, v14
	v_sqrt_f32_e32 v14, v14
	s_nop 0
	v_mul_f32_e32 v9, v9, v14
	ds_write_b32 v47, v8 offset:43712
	v_mul_f32_e32 v9, v157, v9
	v_or_b32_e32 v14, v39, v13
	v_lshl_add_u32 v8, v14, 2, v28
	ds_write_b32 v8, v9
	v_add_f32_e32 v8, v33, v18
	v_mul_f32_e32 v8, 0xbfb8aa3b, v8
	v_exp_f32_e32 v8, v8
	v_add_f32_e32 v9, v32, v10
	v_mul_f32_e32 v9, 0xbfb8aa3b, v9
	v_exp_f32_e32 v9, v9
	v_add_f32_e32 v8, 1.0, v8
	v_rcp_f32_e32 v8, v8
	v_add_f32_e32 v9, 1.0, v9
	v_rcp_f32_e32 v9, v9
	v_mul_f32_e32 v8, 0xc1000000, v8
	v_mul_f32_e32 v8, v12, v8
	v_mul_f32_e32 v8, 0x3fb8aa3b, v8
	v_exp_f32_e32 v8, v8
	s_nop 0
	v_fma_f32 v10, -v8, v8, 1.0
	v_max_f32_e32 v10, 0, v10
	v_sqrt_f32_e32 v10, v10
	s_nop 0
	v_mul_f32_e32 v9, v9, v10
	ds_write_b32 v46, v8 offset:43712
	v_mul_f32_e32 v9, v158, v9
	v_or_b32_e32 v10, v38, v13
	v_lshl_add_u32 v8, v10, 2, v28
	ds_write_b32 v8, v9
	v_add_f32_e32 v8, v33, v19
	v_mul_f32_e32 v8, 0xbfb8aa3b, v8
	v_exp_f32_e32 v8, v8
	v_add_f32_e32 v9, v32, v11
	v_mul_f32_e32 v9, 0xbfb8aa3b, v9
	v_exp_f32_e32 v9, v9
	v_add_f32_e32 v8, 1.0, v8
	v_rcp_f32_e32 v8, v8
	v_add_f32_e32 v9, 1.0, v9
	v_rcp_f32_e32 v9, v9
	v_mul_f32_e32 v8, 0xc1000000, v8
	v_mul_f32_e32 v8, v12, v8
	v_mul_f32_e32 v8, 0x3fb8aa3b, v8
	v_exp_f32_e32 v8, v8
	v_ashrrev_i32_e32 v12, 8, v30
	v_fma_f32 v10, -v8, v8, 1.0
	v_max_f32_e32 v10, 0, v10
	v_sqrt_f32_e32 v10, v10
	s_nop 0
	v_mul_f32_e32 v9, v9, v10
	ds_write_b32 v44, v8 offset:43712
	v_mul_f32_e32 v9, v159, v9
	v_or_b32_e32 v10, v37, v13
	v_lshl_add_u32 v8, v10, 2, v28
	ds_write_b32 v8, v9
	v_bfe_u32 v8, v30, 6, 2
	v_lshlrev_b32_e32 v9, 4, v8
	v_xor_b32_e32 v10, 63, v9
	v_cndmask_b32_e32 v25, v10, v9, vcc
	v_lshl_or_b32 v10, v12, 14, v104
	v_lshl_or_b32 v11, v25, 8, v10
	s_waitcnt lgkmcnt(0)
	s_barrier
	v_add_u32_e32 v13, v111, v11
	v_add_u32_e32 v11, v28, v11
	ds_read_b32 v17, v13 offset:43520
	ds_read_b32 v22, v11
	v_or_b32_e32 v11, 1, v9
	v_xor_b32_e32 v13, 62, v9
	v_cndmask_b32_e32 v19, v13, v11, vcc
	v_lshl_or_b32 v11, v19, 8, v10
	v_add_u32_e32 v13, v111, v11
	v_add_u32_e32 v11, v28, v11
	ds_read_b32 v15, v11
	v_or_b32_e32 v11, 2, v9
	v_xor_b32_e32 v14, 61, v9
	v_cndmask_b32_e32 v20, v14, v11, vcc
	v_lshl_or_b32 v11, v20, 8, v10
	v_add_u32_e32 v14, v111, v11
	v_add_u32_e32 v11, v28, v11
	ds_read_b32 v16, v11
	v_or_b32_e32 v11, 3, v9
	v_xor_b32_e32 v18, 60, v9
	v_cndmask_b32_e32 v21, v18, v11, vcc
	ds_read_b32 v13, v13 offset:43520
	ds_read_b32 v14, v14 offset:43520
	v_lshl_or_b32 v11, v21, 8, v10
	v_add_u32_e32 v18, v111, v11
	v_add_u32_e32 v11, v28, v11
	ds_read_b32 v23, v18 offset:43520
	ds_read_b32 v18, v11
	s_waitcnt lgkmcnt(6)
	v_fmac_f32_e32 v22, 0, v17
	s_waitcnt lgkmcnt(3)
	v_fmac_f32_e32 v15, v22, v13
	v_mul_f32_e32 v13, v17, v13
	s_waitcnt lgkmcnt(2)
	v_fmac_f32_e32 v16, v15, v14
	v_mul_f32_e32 v14, v13, v14
	s_waitcnt lgkmcnt(0)
	v_fmac_f32_e32 v18, v16, v23
	v_mul_f32_e32 v38, v14, v23
	v_or_b32_e32 v11, 4, v9
	v_xor_b32_e32 v23, 59, v9
	v_cndmask_b32_e32 v36, v23, v11, vcc
	v_lshl_or_b32 v11, v36, 8, v10
	v_add_u32_e32 v23, v111, v11
	v_add_u32_e32 v11, v28, v11
	ds_read_b32 v33, v11
	v_or_b32_e32 v11, 5, v9
	v_xor_b32_e32 v24, 58, v9
	v_cndmask_b32_e32 v37, v24, v11, vcc
	v_lshl_or_b32 v11, v37, 8, v10
	v_add_u32_e32 v24, v111, v11
	v_add_u32_e32 v11, v28, v11
	ds_read_b32 v34, v11
	v_or_b32_e32 v11, 6, v9
	v_xor_b32_e32 v32, 57, v9
	v_cndmask_b32_e32 v39, v32, v11, vcc
	ds_read_b32 v23, v23 offset:43520
	ds_read_b32 v24, v24 offset:43520
	v_lshl_or_b32 v11, v39, 8, v10
	v_add_u32_e32 v32, v111, v11
	v_add_u32_e32 v11, v28, v11
	ds_read_b32 v32, v32 offset:43520
	ds_read_b32 v35, v11
	s_waitcnt lgkmcnt(3)
	v_fmac_f32_e32 v33, v18, v23
	v_mul_f32_e32 v23, v38, v23
	s_waitcnt lgkmcnt(2)
	v_fmac_f32_e32 v34, v33, v24
	v_mul_f32_e32 v24, v23, v24
	s_waitcnt lgkmcnt(0)
	v_fmac_f32_e32 v35, v34, v32
	v_mul_f32_e32 v47, v24, v32
	v_or_b32_e32 v11, 7, v9
	v_xor_b32_e32 v32, 56, v9
	v_cndmask_b32_e32 v45, v32, v11, vcc
	v_lshl_or_b32 v11, v45, 8, v10
	v_add_u32_e32 v32, v111, v11
	v_add_u32_e32 v11, v28, v11
	ds_read_b32 v32, v32 offset:43520
	ds_read_b32 v42, v11
	v_or_b32_e32 v11, 8, v9
	s_waitcnt lgkmcnt(1)
	v_mul_f32_e32 v40, v47, v32
	s_waitcnt lgkmcnt(0)
	v_fmac_f32_e32 v42, v35, v32
	v_xor_b32_e32 v32, 55, v9
	v_cndmask_b32_e32 v46, v32, v11, vcc
	v_lshl_or_b32 v11, v46, 8, v10
	v_add_u32_e32 v32, v111, v11
	v_add_u32_e32 v11, v28, v11
	ds_read_b32 v32, v32 offset:43520
	ds_read_b32 v43, v11
	v_or_b32_e32 v11, 9, v9
	s_waitcnt lgkmcnt(1)
	v_mul_f32_e32 v41, v40, v32
	s_waitcnt lgkmcnt(0)
	v_fmac_f32_e32 v43, v42, v32
	v_xor_b32_e32 v32, 54, v9
	v_cndmask_b32_e32 v48, v32, v11, vcc
	v_lshl_or_b32 v11, v48, 8, v10
	v_add_u32_e32 v32, v111, v11
	v_add_u32_e32 v11, v28, v11
	ds_read_b32 v32, v32 offset:43520
	ds_read_b32 v44, v11
	v_or_b32_e32 v11, 10, v9
	s_waitcnt lgkmcnt(1)
	v_mul_f32_e32 v56, v41, v32
	s_waitcnt lgkmcnt(0)
	v_fmac_f32_e32 v44, v43, v32
	v_xor_b32_e32 v32, 53, v9
	v_cndmask_b32_e32 v54, v32, v11, vcc
	v_lshl_or_b32 v11, v54, 8, v10
	v_add_u32_e32 v32, v111, v11
	v_add_u32_e32 v11, v28, v11
	ds_read_b32 v32, v32 offset:43520
	ds_read_b32 v51, v11
	v_or_b32_e32 v11, 11, v9
	s_waitcnt lgkmcnt(1)
	v_mul_f32_e32 v49, v56, v32
	s_waitcnt lgkmcnt(0)
	v_fmac_f32_e32 v51, v44, v32
	v_xor_b32_e32 v32, 52, v9
	v_cndmask_b32_e32 v55, v32, v11, vcc
	v_lshl_or_b32 v11, v55, 8, v10
	v_add_u32_e32 v32, v111, v11
	v_add_u32_e32 v11, v28, v11
	ds_read_b32 v32, v32 offset:43520
	ds_read_b32 v52, v11
	v_or_b32_e32 v11, 12, v9
	s_waitcnt lgkmcnt(1)
	v_mul_f32_e32 v50, v49, v32
	s_waitcnt lgkmcnt(0)
	v_fmac_f32_e32 v52, v51, v32
	v_xor_b32_e32 v32, 51, v9
	v_cndmask_b32_e32 v57, v32, v11, vcc
	v_lshl_or_b32 v11, v57, 8, v10
	v_add_u32_e32 v32, v111, v11
	v_add_u32_e32 v11, v28, v11
	ds_read_b32 v32, v32 offset:43520
	ds_read_b32 v53, v11
	v_or_b32_e32 v11, 13, v9
	s_waitcnt lgkmcnt(1)
	v_mul_f32_e32 v64, v50, v32
	s_waitcnt lgkmcnt(0)
	v_fmac_f32_e32 v53, v52, v32
	v_xor_b32_e32 v32, 50, v9
	v_cndmask_b32_e32 v62, v32, v11, vcc
	v_lshl_or_b32 v11, v62, 8, v10
	v_add_u32_e32 v32, v111, v11
	v_add_u32_e32 v11, v28, v11
	ds_read_b32 v32, v32 offset:43520
	ds_read_b32 v60, v11
	v_or_b32_e32 v11, 14, v9
	s_waitcnt lgkmcnt(1)
	v_mul_f32_e32 v58, v64, v32
	s_waitcnt lgkmcnt(0)
	v_fmac_f32_e32 v60, v53, v32
	v_xor_b32_e32 v32, 49, v9
	v_cndmask_b32_e32 v63, v32, v11, vcc
	v_lshl_or_b32 v11, v63, 8, v10
	v_add_u32_e32 v32, v111, v11
	v_add_u32_e32 v11, v28, v11
	ds_read_b32 v32, v32 offset:43520
	ds_read_b32 v61, v11
	v_or_b32_e32 v11, 15, v9
	v_xor_b32_e32 v9, 48, v9
	v_cndmask_b32_e32 v65, v9, v11, vcc
	v_lshl_or_b32 v9, v65, 8, v10
	v_add_u32_e32 v10, v111, v9
	v_add_u32_e32 v9, v28, v9
	ds_read_b32 v10, v10 offset:43520
	s_waitcnt lgkmcnt(1)
	v_fmac_f32_e32 v61, v60, v32
	v_mul_f32_e32 v59, v58, v32
	ds_read_b32 v32, v9
	v_and_b32_e32 v9, 0x3fffff00, v30
	s_waitcnt lgkmcnt(1)
	v_mul_f32_e32 v66, v59, v10
	v_cmp_ne_u32_e32 vcc, 0, v8
	s_waitcnt lgkmcnt(0)
	v_fmac_f32_e32 v32, v61, v10
	v_lshlrev_b32_e32 v10, 6, v8
	v_or3_b32 v9, v10, v9, v31
	v_lshlrev_b32_e32 v9, 2, v9
	v_add_u32_e32 v10, v27, v9
	v_add_u32_e32 v9, v29, v9
	ds_write_b32 v10, v66
	ds_write_b32 v9, v32
	s_waitcnt lgkmcnt(0)
	s_barrier
	s_and_saveexec_b64 s[0:1], vcc
	s_cbranch_execz .LBB0_372
	v_lshlrev_b32_e32 v9, 2, v30
	v_and_b32_e32 v9, 0xfffffcfc, v9
	v_add_u32_e32 v10, v29, v9
	v_add_u32_e32 v9, v27, v9
	ds_read_b32 v67, v9
	ds_read_b32 v68, v10
	s_waitcnt lgkmcnt(0)
	v_fmac_f32_e32 v68, 0, v67
